# MoE-up SwiGLU epilogue rewritten with packed f32 fma/add/mul and 8-wide instruction-level parallelism (in place in the accumulator registers)
# speedup vs baseline: 1.0149x; 1.0004x over previous
.LBB0_1188:
	s_lshl_b32 s4, s30, 2
	s_add_i32 s4, s4, 0
	s_add_i32 s4, s4, 0x200a0
	v_mov_b32_e32 v0, s4
	v_mbcnt_lo_u32_b32 v10, -1, 0
	v_mbcnt_hi_u32_b32 v10, -1, v10
	ds_read_b32 v0, v0
	s_lshl_b32 s2, s2, 8
	s_lshl_b32 s3, s3, 10
	s_add_i32 s3, s3, 0
	v_pk_add_f32 v[2:3], v[76:77], 1.0 op_sel_hi:[1,0]
	s_waitcnt lgkmcnt(0)
	v_readfirstlane_b32 s4, v0
	v_ashrrev_i32_e32 v0, 1, v10
	s_sub_i32 s2, s4, s2
	v_and_b32_e32 v11, -8, v0
	v_pk_add_f32 v[0:1], v[78:79], 1.0 op_sel_hi:[1,0]
	s_mov_b32 s4, 0xbfd083aa
	v_pk_mul_f32 v[6:7], v[0:1], s[4:5] op_sel_hi:[1,0]
	v_pk_add_f32 v[0:1], v[66:67], 1.0 op_sel_hi:[1,0]
	v_pk_add_f32 v[8:9], v[64:65], 1.0 op_sel_hi:[1,0]
	s_add_i32 s3, s3, 0x20200
	v_pk_mul_f32 v[4:5], v[2:3], s[4:5] op_sel_hi:[1,0]
	v_pk_mul_f32 v[2:3], v[0:1], s[4:5] op_sel_hi:[1,0]
	v_pk_mul_f32 v[0:1], v[8:9], s[4:5] op_sel_hi:[1,0]
	v_and_or_b32 v26, v10, 15, s67
	s_min_i32 s2, s2, 0x100
	v_lshl_add_u32 v18, v26, 2, s3
	ds_read2_b32 v[16:17], v18 offset0:16 offset1:32
	ds_read2_b32 v[14:15], v18 offset0:48 offset1:128
	ds_read2_b32 v[12:13], v18 offset0:144 offset1:160
	ds_read_b32 v10, v18 offset:704
	s_or_b32 s3, s36, s68
	v_add_u32_e32 v8, s3, v11
	v_ashrrev_i32_e32 v9, 31, v8
	v_cmp_gt_i32_e32 vcc, s2, v26
	s_mov_b32 s98, 0xc01d265f
	v_pk_mul_f32 v[20:21], v[72:73], s[98:99] op_sel_hi:[1,0]
	v_pk_mul_f32 v[22:23], v[74:75], s[98:99] op_sel_hi:[1,0]
	v_pk_mul_f32 v[24:25], v[68:69], s[98:99] op_sel_hi:[1,0]
	v_pk_mul_f32 v[248:249], v[70:71], s[98:99] op_sel_hi:[1,0]
	s_mov_b32 s98, 0xbd9d265f
	s_mov_b32 s99, 0xbd5083aa
	v_mov_b32_e32 v27, 0x411c62bf
	s_and_saveexec_b64 s[4:5], vcc
	s_cbranch_execz .LBB0_1190
	ds_read_b32 v18, v18
	v_pk_fma_f32 v[204:205], v[204:205], s[98:99], v[20:21] op_sel_hi:[1,0,1]
	v_pk_fma_f32 v[206:207], v[206:207], s[98:99], v[22:23] op_sel_hi:[1,0,1]
	v_pk_fma_f32 v[196:197], v[196:197], s[98:99], v[24:25] op_sel_hi:[1,0,1]
	v_pk_fma_f32 v[198:199], v[198:199], s[98:99], v[248:249] op_sel_hi:[1,0,1]
	v_pk_fma_f32 v[200:201], v[200:201], s[98:99], v[4:5] op_sel:[0,1,0] op_sel_hi:[1,1,1]
	v_pk_fma_f32 v[202:203], v[202:203], s[98:99], v[6:7] op_sel:[0,1,0] op_sel_hi:[1,1,1]
	v_pk_fma_f32 v[192:193], v[192:193], s[98:99], v[0:1] op_sel:[0,1,0] op_sel_hi:[1,1,1]
	v_pk_fma_f32 v[194:195], v[194:195], s[98:99], v[2:3] op_sel:[0,1,0] op_sel_hi:[1,1,1]
	v_max_f32_e32 v204, 0xc1898193, v204
	v_max_f32_e32 v205, 0xc1898193, v205
	v_max_f32_e32 v206, 0xc1898193, v206
	v_max_f32_e32 v207, 0xc1898193, v207
	v_max_f32_e32 v196, 0xc1898193, v196
	v_max_f32_e32 v197, 0xc1898193, v197
	v_max_f32_e32 v198, 0xc1898193, v198
	v_max_f32_e32 v199, 0xc1898193, v199
	v_exp_f32_e32 v238, v204
	v_exp_f32_e32 v239, v205
	v_exp_f32_e32 v240, v206
	v_exp_f32_e32 v241, v207
	v_exp_f32_e32 v242, v196
	v_exp_f32_e32 v243, v197
	v_exp_f32_e32 v246, v198
	v_exp_f32_e32 v247, v199
	v_med3_f32 v200, v200, s95, v27
	v_med3_f32 v201, v201, s95, v27
	v_med3_f32 v202, v202, s95, v27
	v_med3_f32 v203, v203, s95, v27
	v_med3_f32 v192, v192, s95, v27
	v_med3_f32 v193, v193, s95, v27
	v_med3_f32 v194, v194, s95, v27
	v_med3_f32 v195, v195, s95, v27
	v_pk_add_f32 v[238:239], v[238:239], 1.0 op_sel_hi:[1,0]
	v_pk_add_f32 v[240:241], v[240:241], 1.0 op_sel_hi:[1,0]
	v_pk_add_f32 v[242:243], v[242:243], 1.0 op_sel_hi:[1,0]
	v_pk_add_f32 v[246:247], v[246:247], 1.0 op_sel_hi:[1,0]
	v_rcp_f32_e32 v238, v238
	v_rcp_f32_e32 v239, v239
	v_rcp_f32_e32 v240, v240
	v_rcp_f32_e32 v241, v241
	v_rcp_f32_e32 v242, v242
	v_rcp_f32_e32 v243, v243
	v_rcp_f32_e32 v246, v246
	v_rcp_f32_e32 v247, v247
	s_nop 0
	v_pk_mul_f32 v[204:205], v[204:205], v[238:239]
	v_pk_mul_f32 v[206:207], v[206:207], v[240:241]
	v_pk_mul_f32 v[196:197], v[196:197], v[242:243]
	v_pk_mul_f32 v[198:199], v[198:199], v[246:247]
	v_pk_mul_f32 v[200:201], v[204:205], v[200:201]
	v_pk_mul_f32 v[202:203], v[206:207], v[202:203]
	v_pk_mul_f32 v[192:193], v[196:197], v[192:193]
	v_pk_mul_f32 v[194:195], v[198:199], v[194:195]
	s_waitcnt lgkmcnt(0)
	v_ashrrev_i32_e32 v19, 31, v18
	v_lshlrev_b64 v[18:19], 10, v[18:19]
	v_lshl_add_u64 v[18:19], s[20:21], 0, v[18:19]
	v_lshl_add_u64 v[18:19], v[18:19], 0, v[8:9]
	v_mov_b32_e32 v28, v245
	v_cvt_pk_fp8_f32 v28, v200, v201
	v_mov_b32_e32 v29, v245
	v_cvt_pk_fp8_f32 v29, v192, v193
	v_cvt_pk_fp8_f32 v28, v202, v203 op_sel:[0,0,1]
	v_cvt_pk_fp8_f32 v29, v194, v195 op_sel:[0,0,1]
	global_store_dwordx2 v[18:19], v[28:29], off
.LBB0_1190:
	s_or_b64 exec, exec, s[4:5]
	v_add_u32_e32 v18, 16, v26
	v_cmp_gt_i32_e32 vcc, s2, v18
	s_and_saveexec_b64 s[4:5], vcc
	s_cbranch_execz .LBB0_1192
	v_pk_fma_f32 v[188:189], v[188:189], s[98:99], v[20:21] op_sel_hi:[1,0,1]
	v_pk_fma_f32 v[190:191], v[190:191], s[98:99], v[22:23] op_sel_hi:[1,0,1]
	v_pk_fma_f32 v[180:181], v[180:181], s[98:99], v[24:25] op_sel_hi:[1,0,1]
	v_pk_fma_f32 v[182:183], v[182:183], s[98:99], v[248:249] op_sel_hi:[1,0,1]
	v_pk_fma_f32 v[184:185], v[184:185], s[98:99], v[4:5] op_sel:[0,1,0] op_sel_hi:[1,1,1]
	v_pk_fma_f32 v[186:187], v[186:187], s[98:99], v[6:7] op_sel:[0,1,0] op_sel_hi:[1,1,1]
	v_pk_fma_f32 v[176:177], v[176:177], s[98:99], v[0:1] op_sel:[0,1,0] op_sel_hi:[1,1,1]
	v_pk_fma_f32 v[178:179], v[178:179], s[98:99], v[2:3] op_sel:[0,1,0] op_sel_hi:[1,1,1]
	v_max_f32_e32 v188, 0xc1898193, v188
	v_max_f32_e32 v189, 0xc1898193, v189
	v_max_f32_e32 v190, 0xc1898193, v190
	v_max_f32_e32 v191, 0xc1898193, v191
	v_max_f32_e32 v180, 0xc1898193, v180
	v_max_f32_e32 v181, 0xc1898193, v181
	v_max_f32_e32 v182, 0xc1898193, v182
	v_max_f32_e32 v183, 0xc1898193, v183
	v_exp_f32_e32 v238, v188
	v_exp_f32_e32 v239, v189
	v_exp_f32_e32 v240, v190
	v_exp_f32_e32 v241, v191
	v_exp_f32_e32 v242, v180
	v_exp_f32_e32 v243, v181
	v_exp_f32_e32 v246, v182
	v_exp_f32_e32 v247, v183
	v_med3_f32 v184, v184, s95, v27
	v_med3_f32 v185, v185, s95, v27
	v_med3_f32 v186, v186, s95, v27
	v_med3_f32 v187, v187, s95, v27
	v_med3_f32 v176, v176, s95, v27
	v_med3_f32 v177, v177, s95, v27
	v_med3_f32 v178, v178, s95, v27
	v_med3_f32 v179, v179, s95, v27
	v_pk_add_f32 v[238:239], v[238:239], 1.0 op_sel_hi:[1,0]
	v_pk_add_f32 v[240:241], v[240:241], 1.0 op_sel_hi:[1,0]
	v_pk_add_f32 v[242:243], v[242:243], 1.0 op_sel_hi:[1,0]
	v_pk_add_f32 v[246:247], v[246:247], 1.0 op_sel_hi:[1,0]
	v_rcp_f32_e32 v238, v238
	v_rcp_f32_e32 v239, v239
	v_rcp_f32_e32 v240, v240
	v_rcp_f32_e32 v241, v241
	v_rcp_f32_e32 v242, v242
	v_rcp_f32_e32 v243, v243
	v_rcp_f32_e32 v246, v246
	v_rcp_f32_e32 v247, v247
	s_nop 0
	v_pk_mul_f32 v[188:189], v[188:189], v[238:239]
	v_pk_mul_f32 v[190:191], v[190:191], v[240:241]
	v_pk_mul_f32 v[180:181], v[180:181], v[242:243]
	v_pk_mul_f32 v[182:183], v[182:183], v[246:247]
	v_pk_mul_f32 v[184:185], v[188:189], v[184:185]
	v_pk_mul_f32 v[186:187], v[190:191], v[186:187]
	v_pk_mul_f32 v[176:177], v[180:181], v[176:177]
	v_pk_mul_f32 v[178:179], v[182:183], v[178:179]
	v_mov_b32_e32 v18, v245
	v_cvt_pk_fp8_f32 v18, v184, v185
	v_mov_b32_e32 v19, v245
	v_cvt_pk_fp8_f32 v19, v176, v177
	s_waitcnt lgkmcnt(3)
	v_mov_b32_e32 v28, v16
	v_cvt_pk_fp8_f32 v18, v186, v187 op_sel:[0,0,1]
	v_ashrrev_i32_e32 v29, 31, v16
	v_cvt_pk_fp8_f32 v19, v178, v179 op_sel:[0,0,1]
	v_lshlrev_b64 v[28:29], 10, v[28:29]
	v_lshl_add_u64 v[28:29], s[20:21], 0, v[28:29]
	v_lshl_add_u64 v[28:29], v[28:29], 0, v[8:9]
	global_store_dwordx2 v[28:29], v[18:19], off
.LBB0_1192:
	s_or_b64 exec, exec, s[4:5]
	s_waitcnt lgkmcnt(3)
	v_add_u32_e32 v16, 32, v26
	v_cmp_gt_i32_e32 vcc, s2, v16
	s_and_saveexec_b64 s[4:5], vcc
	s_cbranch_execz .LBB0_1194
	v_pk_fma_f32 v[172:173], v[172:173], s[98:99], v[20:21] op_sel_hi:[1,0,1]
	v_pk_fma_f32 v[174:175], v[174:175], s[98:99], v[22:23] op_sel_hi:[1,0,1]
	v_pk_fma_f32 v[164:165], v[164:165], s[98:99], v[24:25] op_sel_hi:[1,0,1]
	v_pk_fma_f32 v[166:167], v[166:167], s[98:99], v[248:249] op_sel_hi:[1,0,1]
	v_pk_fma_f32 v[168:169], v[168:169], s[98:99], v[4:5] op_sel:[0,1,0] op_sel_hi:[1,1,1]
	v_pk_fma_f32 v[170:171], v[170:171], s[98:99], v[6:7] op_sel:[0,1,0] op_sel_hi:[1,1,1]
	v_pk_fma_f32 v[160:161], v[160:161], s[98:99], v[0:1] op_sel:[0,1,0] op_sel_hi:[1,1,1]
	v_pk_fma_f32 v[162:163], v[162:163], s[98:99], v[2:3] op_sel:[0,1,0] op_sel_hi:[1,1,1]
	v_max_f32_e32 v172, 0xc1898193, v172
	v_max_f32_e32 v173, 0xc1898193, v173
	v_max_f32_e32 v174, 0xc1898193, v174
	v_max_f32_e32 v175, 0xc1898193, v175
	v_max_f32_e32 v164, 0xc1898193, v164
	v_max_f32_e32 v165, 0xc1898193, v165
	v_max_f32_e32 v166, 0xc1898193, v166
	v_max_f32_e32 v167, 0xc1898193, v167
	v_exp_f32_e32 v238, v172
	v_exp_f32_e32 v239, v173
	v_exp_f32_e32 v240, v174
	v_exp_f32_e32 v241, v175
	v_exp_f32_e32 v242, v164
	v_exp_f32_e32 v243, v165
	v_exp_f32_e32 v246, v166
	v_exp_f32_e32 v247, v167
	v_med3_f32 v168, v168, s95, v27
	v_med3_f32 v169, v169, s95, v27
	v_med3_f32 v170, v170, s95, v27
	v_med3_f32 v171, v171, s95, v27
	v_med3_f32 v160, v160, s95, v27
	v_med3_f32 v161, v161, s95, v27
	v_med3_f32 v162, v162, s95, v27
	v_med3_f32 v163, v163, s95, v27
	v_pk_add_f32 v[238:239], v[238:239], 1.0 op_sel_hi:[1,0]
	v_pk_add_f32 v[240:241], v[240:241], 1.0 op_sel_hi:[1,0]
	v_pk_add_f32 v[242:243], v[242:243], 1.0 op_sel_hi:[1,0]
	v_pk_add_f32 v[246:247], v[246:247], 1.0 op_sel_hi:[1,0]
	v_rcp_f32_e32 v238, v238
	v_rcp_f32_e32 v239, v239
	v_rcp_f32_e32 v240, v240
	v_rcp_f32_e32 v241, v241
	v_rcp_f32_e32 v242, v242
	v_rcp_f32_e32 v243, v243
	v_rcp_f32_e32 v246, v246
	v_rcp_f32_e32 v247, v247
	s_nop 0
	v_pk_mul_f32 v[172:173], v[172:173], v[238:239]
	v_pk_mul_f32 v[174:175], v[174:175], v[240:241]
	v_pk_mul_f32 v[164:165], v[164:165], v[242:243]
	v_pk_mul_f32 v[166:167], v[166:167], v[246:247]
	v_pk_mul_f32 v[168:169], v[172:173], v[168:169]
	v_pk_mul_f32 v[170:171], v[174:175], v[170:171]
	v_pk_mul_f32 v[160:161], v[164:165], v[160:161]
	v_pk_mul_f32 v[162:163], v[166:167], v[162:163]
	v_mov_b32_e32 v18, v245
	v_cvt_pk_fp8_f32 v18, v168, v169
	v_mov_b32_e32 v19, v245
	v_cvt_pk_fp8_f32 v19, v160, v161
	v_cvt_pk_fp8_f32 v18, v170, v171 op_sel:[0,0,1]
	v_ashrrev_i32_e32 v29, 31, v17
	v_cvt_pk_fp8_f32 v19, v162, v163 op_sel:[0,0,1]
	v_mov_b32_e32 v28, v17
	v_lshlrev_b64 v[16:17], 10, v[28:29]
	v_lshl_add_u64 v[16:17], s[20:21], 0, v[16:17]
	v_lshl_add_u64 v[16:17], v[16:17], 0, v[8:9]
	global_store_dwordx2 v[16:17], v[18:19], off
.LBB0_1194:
	s_or_b64 exec, exec, s[4:5]
	v_add_u32_e32 v16, 48, v26
	v_cmp_gt_i32_e32 vcc, s2, v16
	s_and_saveexec_b64 s[4:5], vcc
	s_cbranch_execz .LBB0_1196
	v_pk_fma_f32 v[156:157], v[156:157], s[98:99], v[20:21] op_sel_hi:[1,0,1]
	v_pk_fma_f32 v[158:159], v[158:159], s[98:99], v[22:23] op_sel_hi:[1,0,1]
	v_pk_fma_f32 v[148:149], v[148:149], s[98:99], v[24:25] op_sel_hi:[1,0,1]
	v_pk_fma_f32 v[150:151], v[150:151], s[98:99], v[248:249] op_sel_hi:[1,0,1]
	v_pk_fma_f32 v[152:153], v[152:153], s[98:99], v[4:5] op_sel:[0,1,0] op_sel_hi:[1,1,1]
	v_pk_fma_f32 v[154:155], v[154:155], s[98:99], v[6:7] op_sel:[0,1,0] op_sel_hi:[1,1,1]
	v_pk_fma_f32 v[144:145], v[144:145], s[98:99], v[0:1] op_sel:[0,1,0] op_sel_hi:[1,1,1]
	v_pk_fma_f32 v[146:147], v[146:147], s[98:99], v[2:3] op_sel:[0,1,0] op_sel_hi:[1,1,1]
	v_max_f32_e32 v156, 0xc1898193, v156
	v_max_f32_e32 v157, 0xc1898193, v157
	v_max_f32_e32 v158, 0xc1898193, v158
	v_max_f32_e32 v159, 0xc1898193, v159
	v_max_f32_e32 v148, 0xc1898193, v148
	v_max_f32_e32 v149, 0xc1898193, v149
	v_max_f32_e32 v150, 0xc1898193, v150
	v_max_f32_e32 v151, 0xc1898193, v151
	v_exp_f32_e32 v238, v156
	v_exp_f32_e32 v239, v157
	v_exp_f32_e32 v240, v158
	v_exp_f32_e32 v241, v159
	v_exp_f32_e32 v242, v148
	v_exp_f32_e32 v243, v149
	v_exp_f32_e32 v246, v150
	v_exp_f32_e32 v247, v151
	v_med3_f32 v152, v152, s95, v27
	v_med3_f32 v153, v153, s95, v27
	v_med3_f32 v154, v154, s95, v27
	v_med3_f32 v155, v155, s95, v27
	v_med3_f32 v144, v144, s95, v27
	v_med3_f32 v145, v145, s95, v27
	v_med3_f32 v146, v146, s95, v27
	v_med3_f32 v147, v147, s95, v27
	v_pk_add_f32 v[238:239], v[238:239], 1.0 op_sel_hi:[1,0]
	v_pk_add_f32 v[240:241], v[240:241], 1.0 op_sel_hi:[1,0]
	v_pk_add_f32 v[242:243], v[242:243], 1.0 op_sel_hi:[1,0]
	v_pk_add_f32 v[246:247], v[246:247], 1.0 op_sel_hi:[1,0]
	v_rcp_f32_e32 v238, v238
	v_rcp_f32_e32 v239, v239
	v_rcp_f32_e32 v240, v240
	v_rcp_f32_e32 v241, v241
	v_rcp_f32_e32 v242, v242
	v_rcp_f32_e32 v243, v243
	v_rcp_f32_e32 v246, v246
	v_rcp_f32_e32 v247, v247
	s_nop 0
	v_pk_mul_f32 v[156:157], v[156:157], v[238:239]
	v_pk_mul_f32 v[158:159], v[158:159], v[240:241]
	v_pk_mul_f32 v[148:149], v[148:149], v[242:243]
	v_pk_mul_f32 v[150:151], v[150:151], v[246:247]
	v_pk_mul_f32 v[152:153], v[156:157], v[152:153]
	v_pk_mul_f32 v[154:155], v[158:159], v[154:155]
	v_pk_mul_f32 v[144:145], v[148:149], v[144:145]
	v_pk_mul_f32 v[146:147], v[150:151], v[146:147]
	v_mov_b32_e32 v16, v245
	v_cvt_pk_fp8_f32 v16, v152, v153
	v_mov_b32_e32 v17, v245
	v_cvt_pk_fp8_f32 v17, v144, v145
	s_waitcnt lgkmcnt(2)
	v_mov_b32_e32 v18, v14
	v_cvt_pk_fp8_f32 v16, v154, v155 op_sel:[0,0,1]
	v_ashrrev_i32_e32 v19, 31, v14
	v_cvt_pk_fp8_f32 v17, v146, v147 op_sel:[0,0,1]
	v_lshlrev_b64 v[18:19], 10, v[18:19]
	v_lshl_add_u64 v[18:19], s[20:21], 0, v[18:19]
	v_lshl_add_u64 v[18:19], v[18:19], 0, v[8:9]
	global_store_dwordx2 v[18:19], v[16:17], off
.LBB0_1196:
	s_or_b64 exec, exec, s[4:5]
	s_waitcnt lgkmcnt(2)
	v_add_u32_e32 v14, 0x80, v26
	v_cmp_gt_i32_e32 vcc, s2, v14
	s_and_saveexec_b64 s[4:5], vcc
	s_cbranch_execz .LBB0_1198
	v_pk_fma_f32 v[140:141], v[140:141], s[98:99], v[20:21] op_sel_hi:[1,0,1]
	v_pk_fma_f32 v[142:143], v[142:143], s[98:99], v[22:23] op_sel_hi:[1,0,1]
	v_pk_fma_f32 v[132:133], v[132:133], s[98:99], v[24:25] op_sel_hi:[1,0,1]
	v_pk_fma_f32 v[134:135], v[134:135], s[98:99], v[248:249] op_sel_hi:[1,0,1]
	v_pk_fma_f32 v[136:137], v[136:137], s[98:99], v[4:5] op_sel:[0,1,0] op_sel_hi:[1,1,1]
	v_pk_fma_f32 v[138:139], v[138:139], s[98:99], v[6:7] op_sel:[0,1,0] op_sel_hi:[1,1,1]
	v_pk_fma_f32 v[128:129], v[128:129], s[98:99], v[0:1] op_sel:[0,1,0] op_sel_hi:[1,1,1]
	v_pk_fma_f32 v[130:131], v[130:131], s[98:99], v[2:3] op_sel:[0,1,0] op_sel_hi:[1,1,1]
	v_max_f32_e32 v140, 0xc1898193, v140
	v_max_f32_e32 v141, 0xc1898193, v141
	v_max_f32_e32 v142, 0xc1898193, v142
	v_max_f32_e32 v143, 0xc1898193, v143
	v_max_f32_e32 v132, 0xc1898193, v132
	v_max_f32_e32 v133, 0xc1898193, v133
	v_max_f32_e32 v134, 0xc1898193, v134
	v_max_f32_e32 v135, 0xc1898193, v135
	v_exp_f32_e32 v238, v140
	v_exp_f32_e32 v239, v141
	v_exp_f32_e32 v240, v142
	v_exp_f32_e32 v241, v143
	v_exp_f32_e32 v242, v132
	v_exp_f32_e32 v243, v133
	v_exp_f32_e32 v246, v134
	v_exp_f32_e32 v247, v135
	v_med3_f32 v136, v136, s95, v27
	v_med3_f32 v137, v137, s95, v27
	v_med3_f32 v138, v138, s95, v27
	v_med3_f32 v139, v139, s95, v27
	v_med3_f32 v128, v128, s95, v27
	v_med3_f32 v129, v129, s95, v27
	v_med3_f32 v130, v130, s95, v27
	v_med3_f32 v131, v131, s95, v27
	v_pk_add_f32 v[238:239], v[238:239], 1.0 op_sel_hi:[1,0]
	v_pk_add_f32 v[240:241], v[240:241], 1.0 op_sel_hi:[1,0]
	v_pk_add_f32 v[242:243], v[242:243], 1.0 op_sel_hi:[1,0]
	v_pk_add_f32 v[246:247], v[246:247], 1.0 op_sel_hi:[1,0]
	v_rcp_f32_e32 v238, v238
	v_rcp_f32_e32 v239, v239
	v_rcp_f32_e32 v240, v240
	v_rcp_f32_e32 v241, v241
	v_rcp_f32_e32 v242, v242
	v_rcp_f32_e32 v243, v243
	v_rcp_f32_e32 v246, v246
	v_rcp_f32_e32 v247, v247
	s_nop 0
	v_pk_mul_f32 v[140:141], v[140:141], v[238:239]
	v_pk_mul_f32 v[142:143], v[142:143], v[240:241]
	v_pk_mul_f32 v[132:133], v[132:133], v[242:243]
	v_pk_mul_f32 v[134:135], v[134:135], v[246:247]
	v_pk_mul_f32 v[136:137], v[140:141], v[136:137]
	v_pk_mul_f32 v[138:139], v[142:143], v[138:139]
	v_pk_mul_f32 v[128:129], v[132:133], v[128:129]
	v_pk_mul_f32 v[130:131], v[134:135], v[130:131]
	v_mov_b32_e32 v16, v245
	v_cvt_pk_fp8_f32 v16, v136, v137
	v_mov_b32_e32 v17, v245
	v_cvt_pk_fp8_f32 v17, v128, v129
	v_cvt_pk_fp8_f32 v16, v138, v139 op_sel:[0,0,1]
	v_ashrrev_i32_e32 v19, 31, v15
	v_cvt_pk_fp8_f32 v17, v130, v131 op_sel:[0,0,1]
	v_mov_b32_e32 v18, v15
	v_lshlrev_b64 v[14:15], 10, v[18:19]
	v_lshl_add_u64 v[14:15], s[20:21], 0, v[14:15]
	v_lshl_add_u64 v[14:15], v[14:15], 0, v[8:9]
	global_store_dwordx2 v[14:15], v[16:17], off
.LBB0_1198:
	s_or_b64 exec, exec, s[4:5]
	v_add_u32_e32 v14, 0x90, v26
	v_cmp_gt_i32_e32 vcc, s2, v14
	s_and_saveexec_b64 s[4:5], vcc
	s_cbranch_execz .LBB0_1200
	v_pk_fma_f32 v[124:125], v[124:125], s[98:99], v[20:21] op_sel_hi:[1,0,1]
	v_pk_fma_f32 v[126:127], v[126:127], s[98:99], v[22:23] op_sel_hi:[1,0,1]
	v_pk_fma_f32 v[116:117], v[116:117], s[98:99], v[24:25] op_sel_hi:[1,0,1]
	v_pk_fma_f32 v[118:119], v[118:119], s[98:99], v[248:249] op_sel_hi:[1,0,1]
	v_pk_fma_f32 v[120:121], v[120:121], s[98:99], v[4:5] op_sel:[0,1,0] op_sel_hi:[1,1,1]
	v_pk_fma_f32 v[122:123], v[122:123], s[98:99], v[6:7] op_sel:[0,1,0] op_sel_hi:[1,1,1]
	v_pk_fma_f32 v[112:113], v[112:113], s[98:99], v[0:1] op_sel:[0,1,0] op_sel_hi:[1,1,1]
	v_pk_fma_f32 v[114:115], v[114:115], s[98:99], v[2:3] op_sel:[0,1,0] op_sel_hi:[1,1,1]
	v_max_f32_e32 v124, 0xc1898193, v124
	v_max_f32_e32 v125, 0xc1898193, v125
	v_max_f32_e32 v126, 0xc1898193, v126
	v_max_f32_e32 v127, 0xc1898193, v127
	v_max_f32_e32 v116, 0xc1898193, v116
	v_max_f32_e32 v117, 0xc1898193, v117
	v_max_f32_e32 v118, 0xc1898193, v118
	v_max_f32_e32 v119, 0xc1898193, v119
	v_exp_f32_e32 v238, v124
	v_exp_f32_e32 v239, v125
	v_exp_f32_e32 v240, v126
	v_exp_f32_e32 v241, v127
	v_exp_f32_e32 v242, v116
	v_exp_f32_e32 v243, v117
	v_exp_f32_e32 v246, v118
	v_exp_f32_e32 v247, v119
	v_med3_f32 v120, v120, s95, v27
	v_med3_f32 v121, v121, s95, v27
	v_med3_f32 v122, v122, s95, v27
	v_med3_f32 v123, v123, s95, v27
	v_med3_f32 v112, v112, s95, v27
	v_med3_f32 v113, v113, s95, v27
	v_med3_f32 v114, v114, s95, v27
	v_med3_f32 v115, v115, s95, v27
	v_pk_add_f32 v[238:239], v[238:239], 1.0 op_sel_hi:[1,0]
	v_pk_add_f32 v[240:241], v[240:241], 1.0 op_sel_hi:[1,0]
	v_pk_add_f32 v[242:243], v[242:243], 1.0 op_sel_hi:[1,0]
	v_pk_add_f32 v[246:247], v[246:247], 1.0 op_sel_hi:[1,0]
	v_rcp_f32_e32 v238, v238
	v_rcp_f32_e32 v239, v239
	v_rcp_f32_e32 v240, v240
	v_rcp_f32_e32 v241, v241
	v_rcp_f32_e32 v242, v242
	v_rcp_f32_e32 v243, v243
	v_rcp_f32_e32 v246, v246
	v_rcp_f32_e32 v247, v247
	s_nop 0
	v_pk_mul_f32 v[124:125], v[124:125], v[238:239]
	v_pk_mul_f32 v[126:127], v[126:127], v[240:241]
	v_pk_mul_f32 v[116:117], v[116:117], v[242:243]
	v_pk_mul_f32 v[118:119], v[118:119], v[246:247]
	v_pk_mul_f32 v[120:121], v[124:125], v[120:121]
	v_pk_mul_f32 v[122:123], v[126:127], v[122:123]
	v_pk_mul_f32 v[112:113], v[116:117], v[112:113]
	v_pk_mul_f32 v[114:115], v[118:119], v[114:115]
	v_mov_b32_e32 v14, v245
	v_cvt_pk_fp8_f32 v14, v120, v121
	v_mov_b32_e32 v15, v245
	v_cvt_pk_fp8_f32 v15, v112, v113
	s_waitcnt lgkmcnt(1)
	v_mov_b32_e32 v16, v12
	v_cvt_pk_fp8_f32 v14, v122, v123 op_sel:[0,0,1]
	v_ashrrev_i32_e32 v17, 31, v12
	v_cvt_pk_fp8_f32 v15, v114, v115 op_sel:[0,0,1]
	v_lshlrev_b64 v[16:17], 10, v[16:17]
	v_lshl_add_u64 v[16:17], s[20:21], 0, v[16:17]
	v_lshl_add_u64 v[16:17], v[16:17], 0, v[8:9]
	global_store_dwordx2 v[16:17], v[14:15], off
.LBB0_1200:
	s_or_b64 exec, exec, s[4:5]
	s_waitcnt lgkmcnt(1)
	v_add_u32_e32 v12, 0xa0, v26
	v_cmp_gt_i32_e32 vcc, s2, v12
	s_and_saveexec_b64 s[4:5], vcc
	s_cbranch_execz .LBB0_1202
	v_pk_fma_f32 v[108:109], v[108:109], s[98:99], v[20:21] op_sel_hi:[1,0,1]
	v_pk_fma_f32 v[110:111], v[110:111], s[98:99], v[22:23] op_sel_hi:[1,0,1]
	v_pk_fma_f32 v[100:101], v[100:101], s[98:99], v[24:25] op_sel_hi:[1,0,1]
	v_pk_fma_f32 v[102:103], v[102:103], s[98:99], v[248:249] op_sel_hi:[1,0,1]
	v_pk_fma_f32 v[104:105], v[104:105], s[98:99], v[4:5] op_sel:[0,1,0] op_sel_hi:[1,1,1]
	v_pk_fma_f32 v[106:107], v[106:107], s[98:99], v[6:7] op_sel:[0,1,0] op_sel_hi:[1,1,1]
	v_pk_fma_f32 v[96:97], v[96:97], s[98:99], v[0:1] op_sel:[0,1,0] op_sel_hi:[1,1,1]
	v_pk_fma_f32 v[98:99], v[98:99], s[98:99], v[2:3] op_sel:[0,1,0] op_sel_hi:[1,1,1]
	v_max_f32_e32 v108, 0xc1898193, v108
	v_max_f32_e32 v109, 0xc1898193, v109
	v_max_f32_e32 v110, 0xc1898193, v110
	v_max_f32_e32 v111, 0xc1898193, v111
	v_max_f32_e32 v100, 0xc1898193, v100
	v_max_f32_e32 v101, 0xc1898193, v101
	v_max_f32_e32 v102, 0xc1898193, v102
	v_max_f32_e32 v103, 0xc1898193, v103
	v_exp_f32_e32 v238, v108
	v_exp_f32_e32 v239, v109
	v_exp_f32_e32 v240, v110
	v_exp_f32_e32 v241, v111
	v_exp_f32_e32 v242, v100
	v_exp_f32_e32 v243, v101
	v_exp_f32_e32 v246, v102
	v_exp_f32_e32 v247, v103
	v_med3_f32 v104, v104, s95, v27
	v_med3_f32 v105, v105, s95, v27
	v_med3_f32 v106, v106, s95, v27
	v_med3_f32 v107, v107, s95, v27
	v_med3_f32 v96, v96, s95, v27
	v_med3_f32 v97, v97, s95, v27
	v_med3_f32 v98, v98, s95, v27
	v_med3_f32 v99, v99, s95, v27
	v_pk_add_f32 v[238:239], v[238:239], 1.0 op_sel_hi:[1,0]
	v_pk_add_f32 v[240:241], v[240:241], 1.0 op_sel_hi:[1,0]
	v_pk_add_f32 v[242:243], v[242:243], 1.0 op_sel_hi:[1,0]
	v_pk_add_f32 v[246:247], v[246:247], 1.0 op_sel_hi:[1,0]
	v_rcp_f32_e32 v238, v238
	v_rcp_f32_e32 v239, v239
	v_rcp_f32_e32 v240, v240
	v_rcp_f32_e32 v241, v241
	v_rcp_f32_e32 v242, v242
	v_rcp_f32_e32 v243, v243
	v_rcp_f32_e32 v246, v246
	v_rcp_f32_e32 v247, v247
	s_nop 0
	v_pk_mul_f32 v[108:109], v[108:109], v[238:239]
	v_pk_mul_f32 v[110:111], v[110:111], v[240:241]
	v_pk_mul_f32 v[100:101], v[100:101], v[242:243]
	v_pk_mul_f32 v[102:103], v[102:103], v[246:247]
	v_pk_mul_f32 v[104:105], v[108:109], v[104:105]
	v_pk_mul_f32 v[106:107], v[110:111], v[106:107]
	v_pk_mul_f32 v[96:97], v[100:101], v[96:97]
	v_pk_mul_f32 v[98:99], v[102:103], v[98:99]
	v_mov_b32_e32 v14, v245
	v_cvt_pk_fp8_f32 v14, v104, v105
	v_mov_b32_e32 v15, v245
	v_cvt_pk_fp8_f32 v15, v96, v97
	v_cvt_pk_fp8_f32 v14, v106, v107 op_sel:[0,0,1]
	v_ashrrev_i32_e32 v17, 31, v13
	v_cvt_pk_fp8_f32 v15, v98, v99 op_sel:[0,0,1]
	v_mov_b32_e32 v16, v13
	v_lshlrev_b64 v[12:13], 10, v[16:17]
	v_lshl_add_u64 v[12:13], s[20:21], 0, v[12:13]
	v_lshl_add_u64 v[12:13], v[12:13], 0, v[8:9]
	global_store_dwordx2 v[12:13], v[14:15], off
.LBB0_1202:
	s_or_b64 exec, exec, s[4:5]
	v_add_u32_e32 v12, 0xb0, v26
	v_cmp_gt_i32_e32 vcc, s2, v12
	s_and_saveexec_b64 s[4:5], vcc
	s_cbranch_execz .LBB0_1204
	v_pk_fma_f32 v[92:93], v[92:93], s[98:99], v[20:21] op_sel_hi:[1,0,1]
	v_pk_fma_f32 v[94:95], v[94:95], s[98:99], v[22:23] op_sel_hi:[1,0,1]
	v_pk_fma_f32 v[84:85], v[84:85], s[98:99], v[24:25] op_sel_hi:[1,0,1]
	v_pk_fma_f32 v[86:87], v[86:87], s[98:99], v[248:249] op_sel_hi:[1,0,1]
	v_pk_fma_f32 v[88:89], v[88:89], s[98:99], v[4:5] op_sel:[0,1,0] op_sel_hi:[1,1,1]
	v_pk_fma_f32 v[90:91], v[90:91], s[98:99], v[6:7] op_sel:[0,1,0] op_sel_hi:[1,1,1]
	v_pk_fma_f32 v[80:81], v[80:81], s[98:99], v[0:1] op_sel:[0,1,0] op_sel_hi:[1,1,1]
	v_pk_fma_f32 v[82:83], v[82:83], s[98:99], v[2:3] op_sel:[0,1,0] op_sel_hi:[1,1,1]
	v_max_f32_e32 v92, 0xc1898193, v92
	v_max_f32_e32 v93, 0xc1898193, v93
	v_max_f32_e32 v94, 0xc1898193, v94
	v_max_f32_e32 v95, 0xc1898193, v95
	v_max_f32_e32 v84, 0xc1898193, v84
	v_max_f32_e32 v85, 0xc1898193, v85
	v_max_f32_e32 v86, 0xc1898193, v86
	v_max_f32_e32 v87, 0xc1898193, v87
	v_exp_f32_e32 v238, v92
	v_exp_f32_e32 v239, v93
	v_exp_f32_e32 v240, v94
	v_exp_f32_e32 v241, v95
	v_exp_f32_e32 v242, v84
	v_exp_f32_e32 v243, v85
	v_exp_f32_e32 v246, v86
	v_exp_f32_e32 v247, v87
	v_med3_f32 v88, v88, s95, v27
	v_med3_f32 v89, v89, s95, v27
	v_med3_f32 v90, v90, s95, v27
	v_med3_f32 v91, v91, s95, v27
	v_med3_f32 v80, v80, s95, v27
	v_med3_f32 v81, v81, s95, v27
	v_med3_f32 v82, v82, s95, v27
	v_med3_f32 v83, v83, s95, v27
	v_pk_add_f32 v[238:239], v[238:239], 1.0 op_sel_hi:[1,0]
	v_pk_add_f32 v[240:241], v[240:241], 1.0 op_sel_hi:[1,0]
	v_pk_add_f32 v[242:243], v[242:243], 1.0 op_sel_hi:[1,0]
	v_pk_add_f32 v[246:247], v[246:247], 1.0 op_sel_hi:[1,0]
	v_rcp_f32_e32 v238, v238
	v_rcp_f32_e32 v239, v239
	v_rcp_f32_e32 v240, v240
	v_rcp_f32_e32 v241, v241
	v_rcp_f32_e32 v242, v242
	v_rcp_f32_e32 v243, v243
	v_rcp_f32_e32 v246, v246
	v_rcp_f32_e32 v247, v247
	s_nop 0
	v_pk_mul_f32 v[92:93], v[92:93], v[238:239]
	v_pk_mul_f32 v[94:95], v[94:95], v[240:241]
	v_pk_mul_f32 v[84:85], v[84:85], v[242:243]
	v_pk_mul_f32 v[86:87], v[86:87], v[246:247]
	v_pk_mul_f32 v[88:89], v[92:93], v[88:89]
	v_pk_mul_f32 v[90:91], v[94:95], v[90:91]
	v_pk_mul_f32 v[80:81], v[84:85], v[80:81]
	v_pk_mul_f32 v[82:83], v[86:87], v[82:83]
	s_waitcnt lgkmcnt(0)
	v_ashrrev_i32_e32 v11, 31, v10
	v_mov_b32_e32 v0, v245
	v_mov_b32_e32 v1, v245
	v_cvt_pk_fp8_f32 v0, v88, v89
	v_cvt_pk_fp8_f32 v1, v80, v81
	v_cvt_pk_fp8_f32 v0, v90, v91 op_sel:[0,0,1]
	v_cvt_pk_fp8_f32 v1, v82, v83 op_sel:[0,0,1]
	v_lshlrev_b64 v[2:3], 10, v[10:11]
	v_lshl_add_u64 v[2:3], s[20:21], 0, v[2:3]
	v_lshl_add_u64 v[2:3], v[2:3], 0, v[8:9]
	global_store_dwordx2 v[2:3], v[0:1], off
